# baseline (speedup 1.0000x reference)
.LBB1_9:
	s_load_dwordx2 s[18:19], s[0:1], 0x20
	v_and_b32_e32 v101, 63, v0
	s_cmp_lg_u32 s4, 0
	v_lshrrev_b32_e32 v0, 2, v1
	s_cselect_b64 s[20:21], -1, 0
	v_and_or_b32 v100, v102, 12, v0
	s_andn2_b64 vcc, exec, s[8:9]
	s_mov_b32 s17, 0
	s_cbranch_vccnz .LBB1_52
	v_or_b32_e32 v114, 0x20c00, v102
	v_or_b32_e32 v3, 0x20d00, v102
	v_or_b32_e32 v0, 0x20c40, v102
	v_or_b32_e32 v1, 0x20c80, v102
	v_or_b32_e32 v2, 0x20cc0, v102
	v_or_b32_e32 v4, 0x20d40, v102
	v_or_b32_e32 v5, 0x20d80, v102
	v_or_b32_e32 v6, 0x20dc0, v102
	ds_read_b32 v36, v114
	ds_read_b32 v40, v0
	ds_read_b32 v44, v1
	ds_read_b32 v48, v2
	ds_read_b32 v52, v3
	ds_read_b32 v56, v4
	ds_read_b32 v60, v5
	ds_read_b32 v64, v6
	v_lshlrev_b32_e32 v3, 2, v104
	v_lshlrev_b32_e32 v0, 8, v104
	v_lshlrev_b32_e32 v2, 1, v112
	v_and_b32_e32 v4, 12, v3
	s_add_i32 s47, s33, 0x8000
	v_and_b32_e32 v0, 0xf00, v0
	v_bitop3_b32 v3, v2, v3, 12 bitop3:0x78
	v_bitop3_b32 v2, v2, v4, 1 bitop3:0x36
	v_mov_b32_e32 v69, 0
	v_lshlrev_b32_e32 v68, 2, v100
	v_or_b32_e32 v1, s47, v0
	v_lshlrev_b32_e32 v5, 4, v3
	v_lshlrev_b32_e32 v4, 4, v2
	v_and_b32_e32 v6, 48, v104
	v_lshl_add_u64 v[108:109], s[10:11], 0, v[68:69]
	v_add_u32_e32 v0, s33, v0
	s_movk_i32 s0, 0x80
	v_mov_b32_e32 v68, v69
	v_mov_b32_e32 v103, v69
	v_add_u32_e32 v119, v0, v5
	v_add_u32_e32 v120, v0, v4
	v_bitop3_b32 v121, v1, s0, v5 bitop3:0x36
	v_bitop3_b32 v122, v1, s0, v4 bitop3:0x36
	v_mov_b32_e32 v70, v69
	v_mov_b32_e32 v71, v69
	v_add_u32_e32 v123, s43, v6
	v_mov_b64_e32 v[32:33], v[68:69]
	v_mov_b64_e32 v[28:29], v[68:69]
	v_mov_b64_e32 v[24:25], v[68:69]
	v_mov_b64_e32 v[20:21], v[68:69]
	v_mov_b64_e32 v[16:17], v[68:69]
	v_mov_b64_e32 v[12:13], v[68:69]
	v_mov_b64_e32 v[8:9], v[68:69]
	v_mov_b64_e32 v[4:5], v[68:69]
	s_waitcnt lgkmcnt(0)
	v_mov_b32_e32 v37, v36
	v_mov_b32_e32 v38, v36
	v_mov_b32_e32 v39, v36
	v_mov_b32_e32 v41, v40
	v_mov_b32_e32 v42, v40
	v_mov_b32_e32 v43, v40
	v_mov_b32_e32 v45, v44
	v_mov_b32_e32 v46, v44
	v_mov_b32_e32 v47, v44
	v_mov_b32_e32 v49, v48
	v_mov_b32_e32 v50, v48
	v_mov_b32_e32 v51, v48
	v_mov_b32_e32 v53, v52
	v_mov_b32_e32 v54, v52
	v_mov_b32_e32 v55, v52
	v_mov_b32_e32 v57, v56
	v_mov_b32_e32 v58, v56
	v_mov_b32_e32 v59, v56
	v_mov_b32_e32 v61, v60
	v_mov_b32_e32 v62, v60
	v_mov_b32_e32 v63, v60
	v_mov_b32_e32 v65, v64
	v_mov_b32_e32 v66, v64
	v_mov_b32_e32 v67, v64
	v_lshl_add_u64 v[2:3], s[14:15], 0, v[102:103]
	v_lshlrev_b32_e32 v115, 4, v101
	v_lshl_add_u64 v[106:107], s[18:19], 0, v[102:103]
	v_lshlrev_b32_e32 v103, 2, v112
	v_or_b32_e32 v116, 4, v112
	v_or_b32_e32 v117, 8, v112
	v_or_b32_e32 v118, 12, v112
	s_add_i32 s48, s33, 0x8400
	s_add_i32 s49, s33, 0x8800
	s_add_i32 s50, s33, 0x8c00
	s_add_i32 s51, s33, 0x9000
	s_add_i32 s52, s33, 0x9400
	s_add_i32 s53, s33, 0x9800
	s_add_i32 s54, s33, 0x9c00
	v_mov_b32_e32 v1, v100
	s_mov_b32 s45, -1
	s_mov_b32 s16, -16
	s_mov_b32 s14, s6
	s_mov_b32 s15, s7
	v_mov_b32_e32 v124, 0x3727c5ac
	s_movk_i32 s55, 0x4000
	s_mov_b32 s56, 0x24924925
	v_add_u32_e32 v125, 0x400, v114
	v_mov_b32_e32 v126, 0x3f80
	v_mov_b64_e32 v[34:35], v[70:71]
	v_mov_b64_e32 v[30:31], v[70:71]
	v_mov_b64_e32 v[26:27], v[70:71]
	v_mov_b64_e32 v[22:23], v[70:71]
	v_mov_b64_e32 v[18:19], v[70:71]
	v_mov_b64_e32 v[14:15], v[70:71]
	v_mov_b64_e32 v[10:11], v[70:71]
	v_mov_b64_e32 v[6:7], v[70:71]
	v_mov_b32_e32 v0, 0
	s_mov_b32 s46, -1
	s_mov_b32 s64, 1
	s_branch .LBB1_12

.LBB1_12:
	s_mov_b32 s0, s44
	s_add_i32 s44, s44, 1
	s_cmp_ge_u32 s44, s42
	s_cselect_b64 s[22:23], -1, 0
	s_cmp_lt_u32 s44, s42
	s_cselect_b32 s2, s44, s0
	s_waitcnt vmcnt(0)
	s_lshl_b32 s0, s2, 4
	s_mov_b32 s1, s17
	s_mov_b32 m0, s43
	ds_read_b128 v[76:79], v119 offset:32768
	ds_read_b128 v[80:83], v119 offset:36864
	ds_read_b128 v[84:87], v120 offset:32768
	ds_read_b128 v[88:91], v120 offset:36864
	ds_read_b128 v[92:95], v121
	ds_read_b128 v[96:99], v121 offset:4096
	ds_read_b128 v[128:131], v122
	ds_read_b128 v[132:135], v122 offset:4096
	ds_read_b128 v[72:75], v123
	s_waitcnt lgkmcnt(0)
	v_lshl_add_u64 v[70:71], s[0:1], 2, v[2:3]
	global_load_lds_dword v[70:71], off
	ds_read_b128 v[156:159], v115
	ds_read_b128 v[160:163], v115 offset:1024
	ds_read_b128 v[164:167], v115 offset:2048
	v_cvt_pk_bf16_f32 v136, v76, v77
	v_cvt_pk_bf16_f32 v137, v78, v79
	v_cvt_pk_bf16_f32 v138, v84, v85
	v_cvt_pk_bf16_f32 v139, v86, v87
	v_cvt_pk_bf16_f32 v140, v92, v93
	v_cvt_pk_bf16_f32 v141, v94, v95
	v_cvt_pk_bf16_f32 v142, v128, v129
	v_cvt_pk_bf16_f32 v143, v130, v131
	v_cvt_pk_bf16_f32 v144, v80, v81
	v_cvt_pk_bf16_f32 v145, v82, v83
	v_cvt_pk_bf16_f32 v146, v88, v89
	v_cvt_pk_bf16_f32 v147, v90, v91
	v_cvt_pk_bf16_f32 v128, v96, v97
	v_cvt_pk_bf16_f32 v129, v98, v99
	v_cvt_pk_bf16_f32 v130, v132, v133
	v_cvt_pk_bf16_f32 v131, v134, v135
	s_lshl_b32 s0, s2, 13
	s_cmp_lt_u32 s44, s42
	s_cselect_b32 s0, s0, 0x1e848000
	s_mov_b32 s61, s0
	s_add_i32 s63, s44, 1
	s_cmp_eq_u32 s63, s42
	s_cselect_b32 s63, 1, 0
	s_or_b32 s63, s63, s64
	s_mov_b32 s64, 0
	ds_read_b128 v[132:135], v115 offset:3072
	s_waitcnt lgkmcnt(3)
	v_mfma_f32_16x16x32_bf16 v[148:151], v[136:139], v[156:159], v[36:39]
	ds_read_b128 v[156:159], v115 offset:4096
	s_waitcnt lgkmcnt(3)
	v_mfma_f32_16x16x32_bf16 v[152:155], v[136:139], v[160:163], v[40:43]
	ds_read_b128 v[160:163], v115 offset:5120
	s_waitcnt lgkmcnt(3)
	v_mfma_f32_16x16x32_bf16 v[96:99], v[136:139], v[164:167], v[44:47]
	ds_read_b128 v[164:167], v115 offset:6144
	s_waitcnt lgkmcnt(3)
	v_mfma_f32_16x16x32_bf16 v[92:95], v[136:139], v[132:135], v[48:51]
	ds_read_b128 v[132:135], v115 offset:7168
	s_waitcnt lgkmcnt(3)
	v_mfma_f32_16x16x32_bf16 v[88:91], v[136:139], v[156:159], v[52:55]
	ds_read_b128 v[156:159], v115 offset:8192
	s_waitcnt lgkmcnt(3)
	v_mfma_f32_16x16x32_bf16 v[84:87], v[136:139], v[160:163], v[56:59]
	ds_read_b128 v[160:163], v115 offset:9216
	s_waitcnt lgkmcnt(3)
	v_mfma_f32_16x16x32_bf16 v[80:83], v[136:139], v[164:167], v[60:63]
	ds_read_b128 v[164:167], v115 offset:10240
	s_waitcnt lgkmcnt(3)
	v_mfma_f32_16x16x32_bf16 v[76:79], v[136:139], v[132:135], v[64:67]
	ds_read_b128 v[132:135], v115 offset:11264
	s_waitcnt lgkmcnt(3)
	v_mfma_f32_16x16x32_bf16 v[148:151], v[140:143], v[156:159], v[148:151]
	ds_read_b128 v[156:159], v115 offset:12288
	s_waitcnt lgkmcnt(3)
	v_mfma_f32_16x16x32_bf16 v[152:155], v[140:143], v[160:163], v[152:155]
	ds_read_b128 v[160:163], v115 offset:13312
	s_waitcnt lgkmcnt(3)
	v_mfma_f32_16x16x32_bf16 v[96:99], v[140:143], v[164:167], v[96:99]
	ds_read_b128 v[164:167], v115 offset:14336
	s_waitcnt lgkmcnt(3)
	v_mfma_f32_16x16x32_bf16 v[92:95], v[140:143], v[132:135], v[92:95]
	ds_read_b128 v[132:135], v115 offset:15360
	s_waitcnt lgkmcnt(3)
	v_mfma_f32_16x16x32_bf16 v[88:91], v[140:143], v[156:159], v[88:91]
	ds_read_b128 v[156:159], v115 offset:16384
	s_waitcnt lgkmcnt(3)
	v_mfma_f32_16x16x32_bf16 v[84:87], v[140:143], v[160:163], v[84:87]
	ds_read_b128 v[160:163], v115 offset:17408
	s_waitcnt lgkmcnt(3)
	v_mfma_f32_16x16x32_bf16 v[80:83], v[140:143], v[164:167], v[80:83]
	ds_read_b128 v[164:167], v115 offset:18432
	s_waitcnt lgkmcnt(3)
	v_mfma_f32_16x16x32_bf16 v[76:79], v[140:143], v[132:135], v[76:79]
	ds_read_b128 v[132:135], v115 offset:19456
	s_waitcnt lgkmcnt(3)
	s_mov_b32 m0, s47
	s_nop 0
	buffer_load_dwordx4 v113, s[12:15], s61 offen nt lds
	s_cmp_eq_u32 s63, 0
	s_cbranch_scc1 .Lmain_noburst
	s_or_b32 s62, s61, 0x800
	s_mov_b32 m0, s48
	s_nop 0
	buffer_load_dwordx4 v113, s[12:15], s62 offen nt lds
	s_or_b32 s62, s61, 0x1000
	s_mov_b32 m0, s49
	s_nop 0
	buffer_load_dwordx4 v113, s[12:15], s62 offen nt lds
	s_or_b32 s62, s61, 0x1800
	s_mov_b32 m0, s50
	s_nop 0
	buffer_load_dwordx4 v113, s[12:15], s62 offen nt lds
	s_or_b32 s62, s61, 0x100
	s_mov_b32 m0, s51
	s_nop 0
	buffer_load_dwordx4 v113, s[12:15], s62 offen nt lds
	s_or_b32 s62, s61, 0x900
	s_mov_b32 m0, s52
	s_nop 0
	buffer_load_dwordx4 v113, s[12:15], s62 offen nt lds
	s_or_b32 s62, s61, 0x1100
	s_mov_b32 m0, s53
	s_nop 0
	buffer_load_dwordx4 v113, s[12:15], s62 offen nt lds
	s_or_b32 s62, s61, 0x1900
	s_mov_b32 m0, s54
	s_nop 0
	buffer_load_dwordx4 v113, s[12:15], s62 offen nt lds
